# v35 + generic transpose item loads batched + LayerNorm-1 row reductions via DPP row ops and v_readlane instead of ds_bpermute butterflies
# baseline (speedup 1.0000x reference)
.LBB0_1202:
	v_lshl_add_u64 v[78:79], s[18:19], 0, v[60:61]
	s_mov_b32 s10, 0x2f200000
	v_add_co_u32_e32 v4, vcc, s10, v78
	s_mov_b32 s11, 0x2e00000
	s_nop 0
	v_addc_co_u32_e32 v5, vcc, 0, v79, vcc
	s_waitcnt vmcnt(5)
	v_mov_b64_e32 v[8:9], v[124:125]
	v_mov_b64_e32 v[10:11], v[126:127]
	v_mov_b64_e32 v[12:13], v[128:129]
	v_mov_b64_e32 v[14:15], v[130:131]
	v_lshl_add_u64 v[124:125], s[18:19], 0, v[58:59]
	v_add_co_u32_e32 v124, vcc, 0x2f200000, v124
	s_nop 1
	v_addc_co_u32_e32 v125, vcc, 0, v125, vcc
	global_load_dwordx4 v[128:131], v[124:125], off
	global_load_dwordx4 v[124:127], v[124:125], off offset:1024
	s_nop 0
	v_mov_b64_e32 v[4:5], v[160:161]
	v_mov_b64_e32 v[6:7], v[162:163]
	v_add_co_u32_e32 v78, vcc, s11, v78
	s_add_u32 s40, s36, s8
	s_nop 0
	v_addc_co_u32_e32 v79, vcc, 0, v79, vcc
	s_add_u32 s10, s0, s8
	s_addc_u32 s11, s1, s9
	s_add_i32 s41, s40, 0xffffc000
	s_cmpk_lt_i32 s40, 0x4000
	s_cselect_b32 s10, s10, s41
	s_mov_b32 s41, 0x3e200000
	s_cselect_b32 s41, s41, 0x45200000
	s_cselect_b32 s11, s11, 0
	s_add_u32 s41, s18, s41
	s_addc_u32 s42, s19, 0
	s_lshl_b64 s[10:11], s[10:11], 10
	s_add_u32 s10, s41, s10
	s_addc_u32 s11, s42, s11
	v_lshlrev_b32_e32 v62, 16, v8
	v_lshlrev_b32_e32 v70, 16, v12
	v_and_b32_e32 v72, 0xffff0000, v12
	v_add_f32_e32 v2, 0, v70
	v_lshlrev_b32_e32 v71, 16, v13
	v_add_f32_e32 v2, v2, v72
	v_and_b32_e32 v73, 0xffff0000, v13
	v_add_f32_e32 v2, v2, v71
	v_lshlrev_b32_e32 v74, 16, v14
	v_add_f32_e32 v2, v2, v73
	v_and_b32_e32 v76, 0xffff0000, v14
	v_add_f32_e32 v2, v2, v74
	v_lshlrev_b32_e32 v75, 16, v15
	v_add_f32_e32 v2, v2, v76
	v_and_b32_e32 v77, 0xffff0000, v15
	v_add_f32_e32 v2, v2, v75
	v_add_f32_e32 v2, v2, v77
	v_and_b32_e32 v64, 0xffff0000, v8
	v_add_f32_e32 v2, v2, v62
	v_lshlrev_b32_e32 v63, 16, v9
	v_add_f32_e32 v2, v2, v64
	v_and_b32_e32 v65, 0xffff0000, v9
	v_add_f32_e32 v2, v2, v63
	v_lshlrev_b32_e32 v66, 16, v10
	v_add_f32_e32 v2, v2, v65
	v_and_b32_e32 v68, 0xffff0000, v10
	v_add_f32_e32 v2, v2, v66
	v_lshlrev_b32_e32 v67, 16, v11
	v_add_f32_e32 v2, v2, v68
	v_and_b32_e32 v69, 0xffff0000, v11
	v_add_f32_e32 v2, v2, v67
	v_add_f32_e32 v2, v2, v69
	s_nop 1
	v_add_f32_dpp v2, v2, v2 quad_perm:[1,0,3,2] row_mask:0xf bank_mask:0xf
	s_nop 1
	v_add_f32_dpp v2, v2, v2 quad_perm:[2,3,0,1] row_mask:0xf bank_mask:0xf
	s_nop 1
	v_add_f32_dpp v2, v2, v2 row_half_mirror row_mask:0xf bank_mask:0xf
	s_nop 1
	v_add_f32_dpp v2, v2, v2 row_mirror row_mask:0xf bank_mask:0xf
	s_nop 1
	v_add_f32_dpp v2, v2, v2 row_bcast:15 row_mask:0xa bank_mask:0xf
	s_nop 1
	v_add_f32_dpp v2, v2, v2 row_bcast:31 row_mask:0xc bank_mask:0xf
	s_nop 1
	v_readlane_b32 vcc_lo, v2, 63
	s_nop 1
	v_mov_b32_e32 v2, vcc_lo
	v_mov_b64_e32 v[8:9], v[164:165]
	v_mov_b64_e32 v[10:11], v[166:167]
	v_mov_b64_e32 v[12:13], v[168:169]
	v_mov_b64_e32 v[14:15], v[170:171]
	v_mov_b64_e32 v[16:17], v[172:173]
	v_mov_b64_e32 v[18:19], v[174:175]
	v_mov_b64_e32 v[20:21], v[176:177]
	v_mov_b64_e32 v[22:23], v[178:179]
	v_mov_b64_e32 v[24:25], v[180:181]
	v_mov_b64_e32 v[26:27], v[182:183]
	v_mov_b64_e32 v[28:29], v[184:185]
	v_mov_b64_e32 v[30:31], v[186:187]
	v_mov_b64_e32 v[32:33], v[188:189]
	v_mov_b64_e32 v[34:35], v[190:191]
	v_mul_f32_e32 v2, 0x3a800000, v2
	v_pk_add_f32 v[70:71], v[70:71], v[2:3] op_sel_hi:[1,0] neg_lo:[0,1] neg_hi:[0,1]
	v_pk_add_f32 v[72:73], v[72:73], v[2:3] op_sel_hi:[1,0] neg_lo:[0,1] neg_hi:[0,1]
	v_pk_mul_f32 v[108:109], v[70:71], v[70:71]
	v_pk_mul_f32 v[110:111], v[72:73], v[72:73]
	v_pk_add_f32 v[74:75], v[74:75], v[2:3] op_sel_hi:[1,0] neg_lo:[0,1] neg_hi:[0,1]
	v_pk_add_f32 v[76:77], v[76:77], v[2:3] op_sel_hi:[1,0] neg_lo:[0,1] neg_hi:[0,1]
	v_pk_add_f32 v[62:63], v[62:63], v[2:3] op_sel_hi:[1,0] neg_lo:[0,1] neg_hi:[0,1]
	v_pk_add_f32 v[64:65], v[64:65], v[2:3] op_sel_hi:[1,0] neg_lo:[0,1] neg_hi:[0,1]
	v_pk_add_f32 v[66:67], v[66:67], v[2:3] op_sel_hi:[1,0] neg_lo:[0,1] neg_hi:[0,1]
	v_pk_add_f32 v[68:69], v[68:69], v[2:3] op_sel_hi:[1,0] neg_lo:[0,1] neg_hi:[0,1]
	v_add_f32_e32 v2, v108, v110
	v_add_f32_e32 v2, v109, v2
	v_pk_mul_f32 v[112:113], v[74:75], v[74:75]
	v_add_f32_e32 v2, v111, v2
	v_pk_mul_f32 v[114:115], v[76:77], v[76:77]
	v_add_f32_e32 v2, v112, v2
	v_add_f32_e32 v2, v114, v2
	v_add_f32_e32 v2, v113, v2
	v_pk_mul_f32 v[116:117], v[62:63], v[62:63]
	v_add_f32_e32 v2, v115, v2
	v_pk_mul_f32 v[118:119], v[64:65], v[64:65]
	v_add_f32_e32 v2, v116, v2
	v_add_f32_e32 v2, v118, v2
	v_mov_b32_e32 v120, v68
	v_mov_b32_e32 v121, v66
	v_add_f32_e32 v2, v117, v2
	v_pk_mul_f32 v[120:121], v[120:121], v[120:121]
	v_add_f32_e32 v2, v119, v2
	v_mov_b32_e32 v122, v69
	v_mov_b32_e32 v123, v67
	v_add_f32_e32 v2, v121, v2
	v_pk_mul_f32 v[122:123], v[122:123], v[122:123]
	v_add_f32_e32 v2, v120, v2
	v_add_f32_e32 v2, v123, v2
	v_add_f32_e32 v2, v122, v2
	s_nop 1
	v_add_f32_dpp v2, v2, v2 quad_perm:[1,0,3,2] row_mask:0xf bank_mask:0xf
	s_nop 1
	v_add_f32_dpp v2, v2, v2 quad_perm:[2,3,0,1] row_mask:0xf bank_mask:0xf
	s_nop 1
	v_add_f32_dpp v2, v2, v2 row_half_mirror row_mask:0xf bank_mask:0xf
	s_nop 1
	v_add_f32_dpp v2, v2, v2 row_mirror row_mask:0xf bank_mask:0xf
	s_nop 1
	v_add_f32_dpp v2, v2, v2 row_bcast:15 row_mask:0xa bank_mask:0xf
	s_nop 1
	v_add_f32_dpp v2, v2, v2 row_bcast:31 row_mask:0xc bank_mask:0xf
	s_nop 1
	v_readlane_b32 vcc_lo, v2, 63
	s_nop 1
	v_mov_b32_e32 v2, vcc_lo
	v_mov_b32_e32 v108, v4
	v_mov_b32_e32 v109, v6
	v_mov_b32_e32 v6, v5
	v_mov_b32_e32 v110, v8
	v_mov_b32_e32 v111, v10
	v_mov_b32_e32 v10, v9
	v_mov_b32_e32 v8, v16
	v_mov_b32_e32 v4, v12
	v_mov_b32_e32 v5, v14
	v_mov_b32_e32 v9, v18
	v_mov_b32_e32 v12, v24
	v_mov_b32_e32 v14, v13
	v_mov_b32_e32 v18, v17
	v_mov_b32_e32 v13, v26
	v_mov_b32_e32 v16, v32
	v_mov_b32_e32 v17, v34
	v_mov_b32_e32 v26, v25
	v_mov_b32_e32 v34, v33
	v_mov_b32_e32 v24, v20
	v_mov_b32_e32 v25, v22
	v_mov_b32_e32 v32, v28
	v_mov_b32_e32 v33, v30
	v_fmamk_f32 v2, v2, 0x3a800000, v237
	v_mul_f32_e32 v20, 0x4b800000, v2
	v_cmp_gt_f32_e32 vcc, s85, v2
	v_mov_b32_e32 v22, v21
	v_mov_b32_e32 v30, v29
	v_cndmask_b32_e32 v2, v2, v20, vcc
	v_rsq_f32_e32 v2, v2
	s_nop 0
	v_mul_f32_e32 v20, 0x45800000, v2
	v_cndmask_b32_e32 v2, v2, v20, vcc
	v_pk_mul_f32 v[20:21], v[70:71], v[2:3] op_sel_hi:[1,0]
	v_pk_mul_f32 v[28:29], v[74:75], v[2:3] op_sel_hi:[1,0]
	v_pk_mul_f32 v[70:71], v[72:73], v[2:3] op_sel_hi:[1,0]
	v_pk_mul_f32 v[64:65], v[64:65], v[2:3] op_sel_hi:[1,0]
	v_pk_fma_f32 v[12:13], v[12:13], v[20:21], v[16:17]
	v_pk_fma_f32 v[16:17], v[24:25], v[28:29], v[32:33]
	v_pk_fma_f32 v[20:21], v[26:27], v[70:71], v[34:35]
	v_pk_mul_f32 v[72:73], v[76:77], v[2:3] op_sel_hi:[1,0]
	v_pk_fma_f32 v[28:29], v[6:7], v[64:65], v[10:11]
	v_bfe_u32 v6, v20, 16, 1
	v_bfe_u32 v10, v17, 16, 1
	v_max3_f32 v35, |v12|, 0, |v20|
	v_pk_fma_f32 v[22:23], v[22:23], v[72:73], v[30:31]
	v_add3_u32 v53, v20, v6, s86
	v_add3_u32 v6, v17, v10, s86
	v_max3_f32 v10, v35, |v13|, |v21|
	v_pk_mul_f32 v[62:63], v[62:63], v[2:3] op_sel_hi:[1,0]
	v_max3_f32 v10, v10, |v16|, |v22|
	v_pk_fma_f32 v[24:25], v[108:109], v[62:63], v[110:111]
	v_max3_f32 v10, v10, |v17|, |v23|
	v_pk_mul_f32 v[66:67], v[66:67], v[2:3] op_sel_hi:[1,0]
	v_pk_mul_f32 v[68:69], v[68:69], v[2:3] op_sel_hi:[1,0]
	v_max3_f32 v10, v10, |v24|, |v28|
	v_pk_fma_f32 v[26:27], v[4:5], v[66:67], v[8:9]
	v_pk_fma_f32 v[14:15], v[14:15], v[68:69], v[18:19]
	v_max3_f32 v10, v10, |v25|, |v29|
	v_max3_f32 v10, v10, |v26|, |v14|
	v_max3_f32 v10, v10, |v27|, |v15|
	v_mov_b32_e32 v147, v10
	s_nop 1
	v_max_f32_dpp v147, v147, v147 quad_perm:[1,0,3,2] row_mask:0xf bank_mask:0xf
	s_nop 1
	v_max_f32_dpp v147, v147, v147 quad_perm:[2,3,0,1] row_mask:0xf bank_mask:0xf
	s_nop 1
	v_max_f32_dpp v147, v147, v147 row_half_mirror row_mask:0xf bank_mask:0xf
	s_nop 1
	v_max_f32_dpp v147, v147, v147 row_mirror row_mask:0xf bank_mask:0xf
	s_nop 1
	v_max_f32_dpp v147, v147, v147 row_bcast:15 row_mask:0xa bank_mask:0xf
	s_nop 1
	v_max_f32_dpp v147, v147, v147 row_bcast:31 row_mask:0xc bank_mask:0xf
	s_nop 1
	v_readlane_b32 vcc_lo, v147, 63
	s_nop 1
	v_mov_b32_e32 v147, vcc_lo
	v_bfe_u32 v7, v12, 16, 1
	v_add3_u32 v7, v12, v7, s86
	v_lshrrev_b32_e32 v62, 16, v7
	v_bfe_u32 v2, v23, 16, 1
	v_add3_u32 v2, v23, v2, s86
	v_lshrrev_b32_e32 v6, 16, v6
	v_bfe_u32 v8, v13, 16, 1
	v_bfe_u32 v5, v21, 16, 1
	v_add3_u32 v8, v13, v8, s86
	v_bfe_u32 v34, v27, 16, 1
	v_add3_u32 v5, v21, v5, s86
	v_lshrrev_b32_e32 v8, 16, v8
	v_and_or_b32 v7, v2, s87, v6
	v_bfe_u32 v11, v15, 16, 1
	v_add3_u32 v34, v27, v34, s86
	v_and_or_b32 v5, v5, s87, v8
	v_add3_u32 v11, v15, v11, s86
	v_lshrrev_b32_e32 v34, 16, v34
	v_and_or_b32 v11, v11, s87, v34
	v_bfe_u32 v9, v16, 16, 1
	v_bfe_u32 v4, v22, 16, 1
	v_add3_u32 v9, v16, v9, s86
	v_add3_u32 v4, v22, v4, s86
	v_lshrrev_b32_e32 v9, 16, v9
	v_and_or_b32 v6, v4, s87, v9
	v_and_or_b32 v4, v53, s87, v62
	v_max_f32_e32 v2, s55, v147
	global_store_dwordx4 v[78:79], v[4:7], off
	v_bfe_u32 v31, v24, 16, 1
	v_bfe_u32 v32, v25, 16, 1
	v_div_scale_f32 v4, s[42:43], v2, v2, s80
	v_rcp_f32_e32 v5, v4
	v_bfe_u32 v33, v26, 16, 1
	v_bfe_u32 v18, v14, 16, 1
	v_bfe_u32 v19, v29, 16, 1
	v_bfe_u32 v30, v28, 16, 1
	v_add3_u32 v33, v26, v33, s86
	v_add3_u32 v32, v25, v32, s86
	v_add3_u32 v31, v24, v31, s86
	v_fma_f32 v7, -v4, v5, 1.0
	v_add3_u32 v30, v28, v30, s86
	v_add3_u32 v19, v29, v19, s86
	v_add3_u32 v18, v14, v18, s86
	v_lshrrev_b32_e32 v31, 16, v31
	v_lshrrev_b32_e32 v32, 16, v32
	v_lshrrev_b32_e32 v33, 16, v33
	v_div_scale_f32 v6, vcc, s80, v2, s80
	v_fmac_f32_e32 v5, v7, v5
	v_and_or_b32 v10, v18, s87, v33
	v_and_or_b32 v9, v19, s87, v32
	v_and_or_b32 v8, v30, s87, v31
	v_mul_f32_e32 v7, v6, v5
	global_store_dwordx4 v[78:79], v[8:11], off offset:1024
	s_nop 1
	v_fma_f32 v8, -v4, v7, v6
	v_fmac_f32_e32 v7, v8, v5
	v_fma_f32 v4, -v4, v7, v6
	v_div_fmas_f32 v4, v4, v5, v7
	v_div_fixup_f32 v4, v4, v2, s80
	v_mul_f32_e32 v5, v12, v4
	v_mul_f32_e32 v6, v20, v4
	v_rndne_f32_e32 v5, v5
	v_mul_f32_e32 v7, v13, v4
	v_mul_f32_e32 v8, v21, v4
	v_mul_f32_e32 v9, v16, v4
	v_mul_f32_e32 v10, v22, v4
	v_mul_f32_e32 v11, v17, v4
	v_mul_f32_e32 v12, v23, v4
	v_mul_f32_e32 v13, v24, v4
	v_mul_f32_e32 v16, v28, v4
	v_mul_f32_e32 v17, v25, v4
	v_mul_f32_e32 v18, v29, v4
	v_mul_f32_e32 v19, v26, v4
	v_mul_f32_e32 v14, v14, v4
	v_mul_f32_e32 v20, v27, v4
	v_mul_f32_e32 v4, v15, v4
	v_rndne_f32_e32 v6, v6
	v_rndne_f32_e32 v15, v4
	v_add_f32_e32 v4, 0x43000000, v5
	v_rndne_f32_e32 v7, v7
	v_cvt_pk_u8_f32 v4, v4, 0, 0
	v_add_f32_e32 v5, 0x43000000, v6
	v_rndne_f32_e32 v8, v8
	v_cvt_pk_u8_f32 v4, v5, 1, v4
	v_add_f32_e32 v5, 0x43000000, v7
	v_rndne_f32_e32 v9, v9
	v_cvt_pk_u8_f32 v4, v5, 2, v4
	v_add_f32_e32 v5, 0x43000000, v8
	v_rndne_f32_e32 v10, v10
	v_cvt_pk_u8_f32 v4, v5, 3, v4
	v_add_f32_e32 v5, 0x43000000, v9
	v_rndne_f32_e32 v11, v11
	v_cvt_pk_u8_f32 v5, v5, 0, 0
	v_add_f32_e32 v6, 0x43000000, v10
	v_rndne_f32_e32 v12, v12
	v_cvt_pk_u8_f32 v5, v6, 1, v5
	v_add_f32_e32 v6, 0x43000000, v11
	v_rndne_f32_e32 v13, v13
	v_cvt_pk_u8_f32 v5, v6, 2, v5
	v_add_f32_e32 v6, 0x43000000, v12
	v_rndne_f32_e32 v16, v16
	v_cvt_pk_u8_f32 v5, v6, 3, v5
	v_add_f32_e32 v6, 0x43000000, v13
	v_rndne_f32_e32 v17, v17
	v_cvt_pk_u8_f32 v6, v6, 0, 0
	v_add_f32_e32 v7, 0x43000000, v16
	v_rndne_f32_e32 v18, v18
	v_cvt_pk_u8_f32 v6, v7, 1, v6
	v_add_f32_e32 v7, 0x43000000, v17
	v_rndne_f32_e32 v19, v19
	v_cvt_pk_u8_f32 v6, v7, 2, v6
	v_add_f32_e32 v7, 0x43000000, v18
	v_rndne_f32_e32 v14, v14
	v_cvt_pk_u8_f32 v6, v7, 3, v6
	v_add_f32_e32 v7, 0x43000000, v19
	v_rndne_f32_e32 v20, v20
	v_cvt_pk_u8_f32 v7, v7, 0, 0
	v_add_f32_e32 v8, 0x43000000, v14
	v_cvt_pk_u8_f32 v7, v8, 1, v7
	v_add_f32_e32 v8, 0x43000000, v20
	v_cvt_pk_u8_f32 v7, v8, 2, v7
	v_add_f32_e32 v8, 0x43000000, v15
	v_xor_b32_e32 v4, 0x80808080, v4
	v_xor_b32_e32 v5, 0x80808080, v5
	v_cvt_pk_u8_f32 v7, v8, 3, v7
	v_lshl_add_u64 v[8:9], s[10:11], 0, v[38:39]
	v_xor_b32_e32 v6, 0x80808080, v6
	v_xor_b32_e32 v7, 0x80808080, v7
	global_store_dwordx2 v[8:9], v[4:5], off
	global_store_dwordx2 v[8:9], v[6:7], off offset:512
	s_and_saveexec_b64 s[10:11], s[4:5]
	s_cbranch_execz .LBB0_1204
	s_add_u32 s42, s18, s38
	s_addc_u32 s43, s19, s39
	v_mul_f32_e32 v2, 0x3c010204, v2
	global_store_dword v3, v2, s[42:43]
.LBB0_1204:
	s_or_b64 exec, exec, s[10:11]
	v_lshl_add_u64 v[78:79], s[18:19], 0, v[58:59]
	v_add_co_u32_e32 v4, vcc, 0x2f200000, v78
	s_mov_b32 s41, 0x2e00000
	s_nop 0
	v_addc_co_u32_e32 v5, vcc, 0, v79, vcc
	s_waitcnt vmcnt(5)
	v_mov_b64_e32 v[8:9], v[124:125]
	v_mov_b64_e32 v[10:11], v[126:127]
	v_mov_b64_e32 v[12:13], v[128:129]
	v_mov_b64_e32 v[14:15], v[130:131]
	v_lshl_add_u64 v[124:125], s[18:19], 0, v[56:57]
	v_add_co_u32_e32 v124, vcc, 0x2f200000, v124
	s_nop 1
	v_addc_co_u32_e32 v125, vcc, 0, v125, vcc
	global_load_dwordx4 v[128:131], v[124:125], off
	global_load_dwordx4 v[124:127], v[124:125], off offset:1024
	s_nop 0
	v_mov_b64_e32 v[4:5], v[160:161]
	v_mov_b64_e32 v[6:7], v[162:163]
	v_add_co_u32_e32 v78, vcc, s41, v78
	s_add_i32 s10, s40, 1
	s_nop 0
	v_addc_co_u32_e32 v79, vcc, 0, v79, vcc
	s_add_u32 s11, s34, s8
	s_addc_u32 s41, s35, s9
	s_add_i32 s42, s40, 0xffffc001
	s_cmpk_lt_i32 s10, 0x4000
	s_mov_b32 s10, 0x3e200000
	s_cselect_b32 s10, s10, 0x45200000
	s_cselect_b32 s43, s41, 0
	s_cselect_b32 s42, s11, s42
	s_add_u32 s41, s18, s10
	s_addc_u32 s44, s19, 0
	s_lshl_b64 s[10:11], s[42:43], 10
	s_add_u32 s10, s41, s10
	s_addc_u32 s11, s44, s11
	v_lshlrev_b32_e32 v62, 16, v8
	v_lshlrev_b32_e32 v70, 16, v12
	v_and_b32_e32 v72, 0xffff0000, v12
	v_add_f32_e32 v2, 0, v70
	v_lshlrev_b32_e32 v71, 16, v13
	v_add_f32_e32 v2, v2, v72
	v_and_b32_e32 v73, 0xffff0000, v13
	v_add_f32_e32 v2, v2, v71
	v_lshlrev_b32_e32 v74, 16, v14
	v_add_f32_e32 v2, v2, v73
	v_and_b32_e32 v76, 0xffff0000, v14
	v_add_f32_e32 v2, v2, v74
	v_lshlrev_b32_e32 v75, 16, v15
	v_add_f32_e32 v2, v2, v76
	v_and_b32_e32 v77, 0xffff0000, v15
	v_add_f32_e32 v2, v2, v75
	v_add_f32_e32 v2, v2, v77
	v_and_b32_e32 v64, 0xffff0000, v8
	v_add_f32_e32 v2, v2, v62
	v_lshlrev_b32_e32 v63, 16, v9
	v_add_f32_e32 v2, v2, v64
	v_and_b32_e32 v65, 0xffff0000, v9
	v_add_f32_e32 v2, v2, v63
	v_lshlrev_b32_e32 v66, 16, v10
	v_add_f32_e32 v2, v2, v65
	v_and_b32_e32 v68, 0xffff0000, v10
	v_add_f32_e32 v2, v2, v66
	v_lshlrev_b32_e32 v67, 16, v11
	v_add_f32_e32 v2, v2, v68
	v_and_b32_e32 v69, 0xffff0000, v11
	v_add_f32_e32 v2, v2, v67
	v_add_f32_e32 v2, v2, v69
	s_nop 1
	v_add_f32_dpp v2, v2, v2 quad_perm:[1,0,3,2] row_mask:0xf bank_mask:0xf
	s_nop 1
	v_add_f32_dpp v2, v2, v2 quad_perm:[2,3,0,1] row_mask:0xf bank_mask:0xf
	s_nop 1
	v_add_f32_dpp v2, v2, v2 row_half_mirror row_mask:0xf bank_mask:0xf
	s_nop 1
	v_add_f32_dpp v2, v2, v2 row_mirror row_mask:0xf bank_mask:0xf
	s_nop 1
	v_add_f32_dpp v2, v2, v2 row_bcast:15 row_mask:0xa bank_mask:0xf
	s_nop 1
	v_add_f32_dpp v2, v2, v2 row_bcast:31 row_mask:0xc bank_mask:0xf
	s_nop 1
	v_readlane_b32 vcc_lo, v2, 63
	s_nop 1
	v_mov_b32_e32 v2, vcc_lo
	v_mov_b64_e32 v[8:9], v[164:165]
	v_mov_b64_e32 v[10:11], v[166:167]
	v_mov_b64_e32 v[12:13], v[168:169]
	v_mov_b64_e32 v[14:15], v[170:171]
	v_mov_b64_e32 v[16:17], v[172:173]
	v_mov_b64_e32 v[18:19], v[174:175]
	v_mov_b64_e32 v[20:21], v[176:177]
	v_mov_b64_e32 v[22:23], v[178:179]
	v_mov_b64_e32 v[24:25], v[180:181]
	v_mov_b64_e32 v[26:27], v[182:183]
	v_mov_b64_e32 v[28:29], v[184:185]
	v_mov_b64_e32 v[30:31], v[186:187]
	v_mov_b64_e32 v[32:33], v[188:189]
	v_mov_b64_e32 v[34:35], v[190:191]
	v_mul_f32_e32 v2, 0x3a800000, v2
	v_pk_add_f32 v[70:71], v[70:71], v[2:3] op_sel_hi:[1,0] neg_lo:[0,1] neg_hi:[0,1]
	v_pk_add_f32 v[72:73], v[72:73], v[2:3] op_sel_hi:[1,0] neg_lo:[0,1] neg_hi:[0,1]
	v_pk_mul_f32 v[108:109], v[70:71], v[70:71]
	v_pk_mul_f32 v[110:111], v[72:73], v[72:73]
	v_pk_add_f32 v[74:75], v[74:75], v[2:3] op_sel_hi:[1,0] neg_lo:[0,1] neg_hi:[0,1]
	v_pk_add_f32 v[76:77], v[76:77], v[2:3] op_sel_hi:[1,0] neg_lo:[0,1] neg_hi:[0,1]
	v_pk_add_f32 v[62:63], v[62:63], v[2:3] op_sel_hi:[1,0] neg_lo:[0,1] neg_hi:[0,1]
	v_pk_add_f32 v[64:65], v[64:65], v[2:3] op_sel_hi:[1,0] neg_lo:[0,1] neg_hi:[0,1]
	v_pk_add_f32 v[66:67], v[66:67], v[2:3] op_sel_hi:[1,0] neg_lo:[0,1] neg_hi:[0,1]
	v_pk_add_f32 v[68:69], v[68:69], v[2:3] op_sel_hi:[1,0] neg_lo:[0,1] neg_hi:[0,1]
	v_add_f32_e32 v2, v108, v110
	v_add_f32_e32 v2, v109, v2
	v_pk_mul_f32 v[112:113], v[74:75], v[74:75]
	v_add_f32_e32 v2, v111, v2
	v_pk_mul_f32 v[114:115], v[76:77], v[76:77]
	v_add_f32_e32 v2, v112, v2
	v_add_f32_e32 v2, v114, v2
	v_add_f32_e32 v2, v113, v2
	v_pk_mul_f32 v[116:117], v[62:63], v[62:63]
	v_add_f32_e32 v2, v115, v2
	v_pk_mul_f32 v[118:119], v[64:65], v[64:65]
	v_add_f32_e32 v2, v116, v2
	v_add_f32_e32 v2, v118, v2
	v_mov_b32_e32 v120, v68
	v_mov_b32_e32 v121, v66
	v_add_f32_e32 v2, v117, v2
	v_pk_mul_f32 v[120:121], v[120:121], v[120:121]
	v_add_f32_e32 v2, v119, v2
	v_mov_b32_e32 v122, v69
	v_mov_b32_e32 v123, v67
	v_add_f32_e32 v2, v121, v2
	v_pk_mul_f32 v[122:123], v[122:123], v[122:123]
	v_add_f32_e32 v2, v120, v2
	v_add_f32_e32 v2, v123, v2
	v_add_f32_e32 v2, v122, v2
	s_nop 1
	v_add_f32_dpp v2, v2, v2 quad_perm:[1,0,3,2] row_mask:0xf bank_mask:0xf
	s_nop 1
	v_add_f32_dpp v2, v2, v2 quad_perm:[2,3,0,1] row_mask:0xf bank_mask:0xf
	s_nop 1
	v_add_f32_dpp v2, v2, v2 row_half_mirror row_mask:0xf bank_mask:0xf
	s_nop 1
	v_add_f32_dpp v2, v2, v2 row_mirror row_mask:0xf bank_mask:0xf
	s_nop 1
	v_add_f32_dpp v2, v2, v2 row_bcast:15 row_mask:0xa bank_mask:0xf
	s_nop 1
	v_add_f32_dpp v2, v2, v2 row_bcast:31 row_mask:0xc bank_mask:0xf
	s_nop 1
	v_readlane_b32 vcc_lo, v2, 63
	s_nop 1
	v_mov_b32_e32 v2, vcc_lo
	v_mov_b32_e32 v108, v4
	v_mov_b32_e32 v109, v6
	v_mov_b32_e32 v6, v5
	v_mov_b32_e32 v110, v8
	v_mov_b32_e32 v111, v10
	v_mov_b32_e32 v10, v9
	v_mov_b32_e32 v8, v16
	v_mov_b32_e32 v4, v12
	v_mov_b32_e32 v5, v14
	v_mov_b32_e32 v9, v18
	v_mov_b32_e32 v12, v24
	v_mov_b32_e32 v14, v13
	v_mov_b32_e32 v18, v17
	v_mov_b32_e32 v13, v26
	v_mov_b32_e32 v16, v32
	v_mov_b32_e32 v17, v34
	v_mov_b32_e32 v26, v25
	v_mov_b32_e32 v34, v33
	v_mov_b32_e32 v24, v20
	v_mov_b32_e32 v25, v22
	v_mov_b32_e32 v32, v28
	v_mov_b32_e32 v33, v30
	v_fmamk_f32 v2, v2, 0x3a800000, v237
	v_mul_f32_e32 v20, 0x4b800000, v2
	v_cmp_gt_f32_e32 vcc, s85, v2
	v_mov_b32_e32 v22, v21
	v_mov_b32_e32 v30, v29
	v_cndmask_b32_e32 v2, v2, v20, vcc
	v_rsq_f32_e32 v2, v2
	s_nop 0
	v_mul_f32_e32 v20, 0x45800000, v2
	v_cndmask_b32_e32 v2, v2, v20, vcc
	v_pk_mul_f32 v[20:21], v[70:71], v[2:3] op_sel_hi:[1,0]
	v_pk_mul_f32 v[28:29], v[74:75], v[2:3] op_sel_hi:[1,0]
	v_pk_mul_f32 v[70:71], v[72:73], v[2:3] op_sel_hi:[1,0]
	v_pk_mul_f32 v[64:65], v[64:65], v[2:3] op_sel_hi:[1,0]
	v_pk_fma_f32 v[12:13], v[12:13], v[20:21], v[16:17]
	v_pk_fma_f32 v[16:17], v[24:25], v[28:29], v[32:33]
	v_pk_fma_f32 v[20:21], v[26:27], v[70:71], v[34:35]
	v_pk_mul_f32 v[72:73], v[76:77], v[2:3] op_sel_hi:[1,0]
	v_pk_fma_f32 v[28:29], v[6:7], v[64:65], v[10:11]
	v_bfe_u32 v6, v20, 16, 1
	v_bfe_u32 v10, v17, 16, 1
	v_max3_f32 v35, |v12|, 0, |v20|
	v_pk_fma_f32 v[22:23], v[22:23], v[72:73], v[30:31]
	v_add3_u32 v53, v20, v6, s86
	v_add3_u32 v6, v17, v10, s86
	v_max3_f32 v10, v35, |v13|, |v21|
	v_pk_mul_f32 v[62:63], v[62:63], v[2:3] op_sel_hi:[1,0]
	v_max3_f32 v10, v10, |v16|, |v22|
	v_pk_fma_f32 v[24:25], v[108:109], v[62:63], v[110:111]
	v_max3_f32 v10, v10, |v17|, |v23|
	v_pk_mul_f32 v[66:67], v[66:67], v[2:3] op_sel_hi:[1,0]
	v_pk_mul_f32 v[68:69], v[68:69], v[2:3] op_sel_hi:[1,0]
	v_max3_f32 v10, v10, |v24|, |v28|
	v_pk_fma_f32 v[26:27], v[4:5], v[66:67], v[8:9]
	v_pk_fma_f32 v[14:15], v[14:15], v[68:69], v[18:19]
	v_max3_f32 v10, v10, |v25|, |v29|
	v_max3_f32 v10, v10, |v26|, |v14|
	v_max3_f32 v10, v10, |v27|, |v15|
	v_mov_b32_e32 v147, v10
	s_nop 1
	v_max_f32_dpp v147, v147, v147 quad_perm:[1,0,3,2] row_mask:0xf bank_mask:0xf
	s_nop 1
	v_max_f32_dpp v147, v147, v147 quad_perm:[2,3,0,1] row_mask:0xf bank_mask:0xf
	s_nop 1
	v_max_f32_dpp v147, v147, v147 row_half_mirror row_mask:0xf bank_mask:0xf
	s_nop 1
	v_max_f32_dpp v147, v147, v147 row_mirror row_mask:0xf bank_mask:0xf
	s_nop 1
	v_max_f32_dpp v147, v147, v147 row_bcast:15 row_mask:0xa bank_mask:0xf
	s_nop 1
	v_max_f32_dpp v147, v147, v147 row_bcast:31 row_mask:0xc bank_mask:0xf
	s_nop 1
	v_readlane_b32 vcc_lo, v147, 63
	s_nop 1
	v_mov_b32_e32 v147, vcc_lo
	v_bfe_u32 v7, v12, 16, 1
	v_add3_u32 v7, v12, v7, s86
	v_lshrrev_b32_e32 v62, 16, v7
	v_bfe_u32 v2, v23, 16, 1
	v_add3_u32 v2, v23, v2, s86
	v_lshrrev_b32_e32 v6, 16, v6
	v_bfe_u32 v8, v13, 16, 1
	v_bfe_u32 v5, v21, 16, 1
	v_add3_u32 v8, v13, v8, s86
	v_bfe_u32 v34, v27, 16, 1
	v_add3_u32 v5, v21, v5, s86
	v_lshrrev_b32_e32 v8, 16, v8
	v_and_or_b32 v7, v2, s87, v6
	v_bfe_u32 v11, v15, 16, 1
	v_add3_u32 v34, v27, v34, s86
	v_and_or_b32 v5, v5, s87, v8
	v_add3_u32 v11, v15, v11, s86
	v_lshrrev_b32_e32 v34, 16, v34
	v_and_or_b32 v11, v11, s87, v34
	v_bfe_u32 v9, v16, 16, 1
	v_bfe_u32 v4, v22, 16, 1
	v_add3_u32 v9, v16, v9, s86
	v_add3_u32 v4, v22, v4, s86
	v_lshrrev_b32_e32 v9, 16, v9
	v_and_or_b32 v6, v4, s87, v9
	v_and_or_b32 v4, v53, s87, v62
	v_max_f32_e32 v2, s55, v147
	global_store_dwordx4 v[78:79], v[4:7], off
	v_bfe_u32 v31, v24, 16, 1
	v_bfe_u32 v32, v25, 16, 1
	v_div_scale_f32 v4, s[42:43], v2, v2, s80
	v_rcp_f32_e32 v5, v4
	v_bfe_u32 v33, v26, 16, 1
	v_bfe_u32 v18, v14, 16, 1
	v_bfe_u32 v19, v29, 16, 1
	v_bfe_u32 v30, v28, 16, 1
	v_add3_u32 v33, v26, v33, s86
	v_add3_u32 v32, v25, v32, s86
	v_add3_u32 v31, v24, v31, s86
	v_fma_f32 v7, -v4, v5, 1.0
	v_add3_u32 v30, v28, v30, s86
	v_add3_u32 v19, v29, v19, s86
	v_add3_u32 v18, v14, v18, s86
	v_lshrrev_b32_e32 v31, 16, v31
	v_lshrrev_b32_e32 v32, 16, v32
	v_lshrrev_b32_e32 v33, 16, v33
	v_div_scale_f32 v6, vcc, s80, v2, s80
	v_fmac_f32_e32 v5, v7, v5
	v_and_or_b32 v10, v18, s87, v33
	v_and_or_b32 v9, v19, s87, v32
	v_and_or_b32 v8, v30, s87, v31
	v_mul_f32_e32 v7, v6, v5
	global_store_dwordx4 v[78:79], v[8:11], off offset:1024
	s_nop 1
	v_fma_f32 v8, -v4, v7, v6
	v_fmac_f32_e32 v7, v8, v5
	v_fma_f32 v4, -v4, v7, v6
	v_div_fmas_f32 v4, v4, v5, v7
	v_div_fixup_f32 v4, v4, v2, s80
	v_mul_f32_e32 v5, v12, v4
	v_mul_f32_e32 v6, v20, v4
	v_rndne_f32_e32 v5, v5
	v_mul_f32_e32 v7, v13, v4
	v_mul_f32_e32 v8, v21, v4
	v_mul_f32_e32 v9, v16, v4
	v_mul_f32_e32 v10, v22, v4
	v_mul_f32_e32 v11, v17, v4
	v_mul_f32_e32 v12, v23, v4
	v_mul_f32_e32 v13, v24, v4
	v_mul_f32_e32 v16, v28, v4
	v_mul_f32_e32 v17, v25, v4
	v_mul_f32_e32 v18, v29, v4
	v_mul_f32_e32 v19, v26, v4
	v_mul_f32_e32 v14, v14, v4
	v_mul_f32_e32 v20, v27, v4
	v_mul_f32_e32 v4, v15, v4
	v_rndne_f32_e32 v6, v6
	v_rndne_f32_e32 v15, v4
	v_add_f32_e32 v4, 0x43000000, v5
	v_rndne_f32_e32 v7, v7
	v_cvt_pk_u8_f32 v4, v4, 0, 0
	v_add_f32_e32 v5, 0x43000000, v6
	v_rndne_f32_e32 v8, v8
	v_cvt_pk_u8_f32 v4, v5, 1, v4
	v_add_f32_e32 v5, 0x43000000, v7
	v_rndne_f32_e32 v9, v9
	v_cvt_pk_u8_f32 v4, v5, 2, v4
	v_add_f32_e32 v5, 0x43000000, v8
	v_rndne_f32_e32 v10, v10
	v_cvt_pk_u8_f32 v4, v5, 3, v4
	v_add_f32_e32 v5, 0x43000000, v9
	v_rndne_f32_e32 v11, v11
	v_cvt_pk_u8_f32 v5, v5, 0, 0
	v_add_f32_e32 v6, 0x43000000, v10
	v_rndne_f32_e32 v12, v12
	v_cvt_pk_u8_f32 v5, v6, 1, v5
	v_add_f32_e32 v6, 0x43000000, v11
	v_rndne_f32_e32 v13, v13
	v_cvt_pk_u8_f32 v5, v6, 2, v5
	v_add_f32_e32 v6, 0x43000000, v12
	v_rndne_f32_e32 v16, v16
	v_cvt_pk_u8_f32 v5, v6, 3, v5
	v_add_f32_e32 v6, 0x43000000, v13
	v_rndne_f32_e32 v17, v17
	v_cvt_pk_u8_f32 v6, v6, 0, 0
	v_add_f32_e32 v7, 0x43000000, v16
	v_rndne_f32_e32 v18, v18
	v_cvt_pk_u8_f32 v6, v7, 1, v6
	v_add_f32_e32 v7, 0x43000000, v17
	v_rndne_f32_e32 v19, v19
	v_cvt_pk_u8_f32 v6, v7, 2, v6
	v_add_f32_e32 v7, 0x43000000, v18
	v_rndne_f32_e32 v14, v14
	v_cvt_pk_u8_f32 v6, v7, 3, v6
	v_add_f32_e32 v7, 0x43000000, v19
	v_rndne_f32_e32 v20, v20
	v_cvt_pk_u8_f32 v7, v7, 0, 0
	v_add_f32_e32 v8, 0x43000000, v14
	v_cvt_pk_u8_f32 v7, v8, 1, v7
	v_add_f32_e32 v8, 0x43000000, v20
	v_cvt_pk_u8_f32 v7, v8, 2, v7
	v_add_f32_e32 v8, 0x43000000, v15
	v_xor_b32_e32 v4, 0x80808080, v4
	v_xor_b32_e32 v5, 0x80808080, v5
	v_cvt_pk_u8_f32 v7, v8, 3, v7
	v_lshl_add_u64 v[8:9], s[10:11], 0, v[38:39]
	v_xor_b32_e32 v6, 0x80808080, v6
	v_xor_b32_e32 v7, 0x80808080, v7
	global_store_dwordx2 v[8:9], v[4:5], off
	global_store_dwordx2 v[8:9], v[6:7], off offset:512
	s_and_saveexec_b64 s[10:11], s[4:5]
	s_cbranch_execz .LBB0_1206
	s_add_u32 s42, s18, s16
	s_addc_u32 s43, s19, s17
	v_mul_f32_e32 v2, 0x3c010204, v2
	global_store_dword v3, v2, s[42:43]
.LBB0_1206:
	s_or_b64 exec, exec, s[10:11]
	v_lshl_add_u64 v[78:79], s[18:19], 0, v[56:57]
	v_add_co_u32_e32 v4, vcc, 0x2f200000, v78
	s_mov_b32 s41, 0x2e00000
	s_nop 0
	v_addc_co_u32_e32 v5, vcc, 0, v79, vcc
	s_waitcnt vmcnt(5)
	v_mov_b64_e32 v[8:9], v[124:125]
	v_mov_b64_e32 v[10:11], v[126:127]
	v_mov_b64_e32 v[12:13], v[128:129]
	v_mov_b64_e32 v[14:15], v[130:131]
	v_lshl_add_u64 v[124:125], s[18:19], 0, v[54:55]
	v_add_co_u32_e32 v124, vcc, 0x2f200000, v124
	s_nop 1
	v_addc_co_u32_e32 v125, vcc, 0, v125, vcc
	global_load_dwordx4 v[128:131], v[124:125], off
	global_load_dwordx4 v[124:127], v[124:125], off offset:1024
	s_nop 0
	v_mov_b64_e32 v[4:5], v[160:161]
	v_mov_b64_e32 v[6:7], v[162:163]
	v_add_co_u32_e32 v78, vcc, s41, v78
	s_add_i32 s10, s40, 2
	s_nop 0
	v_addc_co_u32_e32 v79, vcc, 0, v79, vcc
	s_add_u32 s11, s30, s8
	s_addc_u32 s41, s31, s9
	s_add_i32 s42, s40, 0xffffc002
	s_cmpk_lt_i32 s10, 0x4000
	s_mov_b32 s10, 0x3e200000
	s_cselect_b32 s10, s10, 0x45200000
	s_cselect_b32 s43, s41, 0
	s_cselect_b32 s42, s11, s42
	s_add_u32 s41, s18, s10
	s_addc_u32 s44, s19, 0
	s_lshl_b64 s[10:11], s[42:43], 10
	s_add_u32 s10, s41, s10
	s_addc_u32 s11, s44, s11
	v_lshlrev_b32_e32 v62, 16, v8
	v_lshlrev_b32_e32 v70, 16, v12
	v_and_b32_e32 v72, 0xffff0000, v12
	v_add_f32_e32 v2, 0, v70
	v_lshlrev_b32_e32 v71, 16, v13
	v_add_f32_e32 v2, v2, v72
	v_and_b32_e32 v73, 0xffff0000, v13
	v_add_f32_e32 v2, v2, v71
	v_lshlrev_b32_e32 v74, 16, v14
	v_add_f32_e32 v2, v2, v73
	v_and_b32_e32 v76, 0xffff0000, v14
	v_add_f32_e32 v2, v2, v74
	v_lshlrev_b32_e32 v75, 16, v15
	v_add_f32_e32 v2, v2, v76
	v_and_b32_e32 v77, 0xffff0000, v15
	v_add_f32_e32 v2, v2, v75
	v_add_f32_e32 v2, v2, v77
	v_and_b32_e32 v64, 0xffff0000, v8
	v_add_f32_e32 v2, v2, v62
	v_lshlrev_b32_e32 v63, 16, v9
	v_add_f32_e32 v2, v2, v64
	v_and_b32_e32 v65, 0xffff0000, v9
	v_add_f32_e32 v2, v2, v63
	v_lshlrev_b32_e32 v66, 16, v10
	v_add_f32_e32 v2, v2, v65
	v_and_b32_e32 v68, 0xffff0000, v10
	v_add_f32_e32 v2, v2, v66
	v_lshlrev_b32_e32 v67, 16, v11
	v_add_f32_e32 v2, v2, v68
	v_and_b32_e32 v69, 0xffff0000, v11
	v_add_f32_e32 v2, v2, v67
	v_add_f32_e32 v2, v2, v69
	s_nop 1
	v_add_f32_dpp v2, v2, v2 quad_perm:[1,0,3,2] row_mask:0xf bank_mask:0xf
	s_nop 1
	v_add_f32_dpp v2, v2, v2 quad_perm:[2,3,0,1] row_mask:0xf bank_mask:0xf
	s_nop 1
	v_add_f32_dpp v2, v2, v2 row_half_mirror row_mask:0xf bank_mask:0xf
	s_nop 1
	v_add_f32_dpp v2, v2, v2 row_mirror row_mask:0xf bank_mask:0xf
	s_nop 1
	v_add_f32_dpp v2, v2, v2 row_bcast:15 row_mask:0xa bank_mask:0xf
	s_nop 1
	v_add_f32_dpp v2, v2, v2 row_bcast:31 row_mask:0xc bank_mask:0xf
	s_nop 1
	v_readlane_b32 vcc_lo, v2, 63
	s_nop 1
	v_mov_b32_e32 v2, vcc_lo
	v_mov_b64_e32 v[8:9], v[164:165]
	v_mov_b64_e32 v[10:11], v[166:167]
	v_mov_b64_e32 v[12:13], v[168:169]
	v_mov_b64_e32 v[14:15], v[170:171]
	v_mov_b64_e32 v[16:17], v[172:173]
	v_mov_b64_e32 v[18:19], v[174:175]
	v_mov_b64_e32 v[20:21], v[176:177]
	v_mov_b64_e32 v[22:23], v[178:179]
	v_mov_b64_e32 v[24:25], v[180:181]
	v_mov_b64_e32 v[26:27], v[182:183]
	v_mov_b64_e32 v[28:29], v[184:185]
	v_mov_b64_e32 v[30:31], v[186:187]
	v_mov_b64_e32 v[32:33], v[188:189]
	v_mov_b64_e32 v[34:35], v[190:191]
	v_mul_f32_e32 v2, 0x3a800000, v2
	v_pk_add_f32 v[70:71], v[70:71], v[2:3] op_sel_hi:[1,0] neg_lo:[0,1] neg_hi:[0,1]
	v_pk_add_f32 v[72:73], v[72:73], v[2:3] op_sel_hi:[1,0] neg_lo:[0,1] neg_hi:[0,1]
	v_pk_mul_f32 v[108:109], v[70:71], v[70:71]
	v_pk_mul_f32 v[110:111], v[72:73], v[72:73]
	v_pk_add_f32 v[74:75], v[74:75], v[2:3] op_sel_hi:[1,0] neg_lo:[0,1] neg_hi:[0,1]
	v_pk_add_f32 v[76:77], v[76:77], v[2:3] op_sel_hi:[1,0] neg_lo:[0,1] neg_hi:[0,1]
	v_pk_add_f32 v[62:63], v[62:63], v[2:3] op_sel_hi:[1,0] neg_lo:[0,1] neg_hi:[0,1]
	v_pk_add_f32 v[64:65], v[64:65], v[2:3] op_sel_hi:[1,0] neg_lo:[0,1] neg_hi:[0,1]
	v_pk_add_f32 v[66:67], v[66:67], v[2:3] op_sel_hi:[1,0] neg_lo:[0,1] neg_hi:[0,1]
	v_pk_add_f32 v[68:69], v[68:69], v[2:3] op_sel_hi:[1,0] neg_lo:[0,1] neg_hi:[0,1]
	v_add_f32_e32 v2, v108, v110
	v_add_f32_e32 v2, v109, v2
	v_pk_mul_f32 v[112:113], v[74:75], v[74:75]
	v_add_f32_e32 v2, v111, v2
	v_pk_mul_f32 v[114:115], v[76:77], v[76:77]
	v_add_f32_e32 v2, v112, v2
	v_add_f32_e32 v2, v114, v2
	v_add_f32_e32 v2, v113, v2
	v_pk_mul_f32 v[116:117], v[62:63], v[62:63]
	v_add_f32_e32 v2, v115, v2
	v_pk_mul_f32 v[118:119], v[64:65], v[64:65]
	v_add_f32_e32 v2, v116, v2
	v_add_f32_e32 v2, v118, v2
	v_mov_b32_e32 v120, v68
	v_mov_b32_e32 v121, v66
	v_add_f32_e32 v2, v117, v2
	v_pk_mul_f32 v[120:121], v[120:121], v[120:121]
	v_add_f32_e32 v2, v119, v2
	v_mov_b32_e32 v122, v69
	v_mov_b32_e32 v123, v67
	v_add_f32_e32 v2, v121, v2
	v_pk_mul_f32 v[122:123], v[122:123], v[122:123]
	v_add_f32_e32 v2, v120, v2
	v_add_f32_e32 v2, v123, v2
	v_add_f32_e32 v2, v122, v2
	s_nop 1
	v_add_f32_dpp v2, v2, v2 quad_perm:[1,0,3,2] row_mask:0xf bank_mask:0xf
	s_nop 1
	v_add_f32_dpp v2, v2, v2 quad_perm:[2,3,0,1] row_mask:0xf bank_mask:0xf
	s_nop 1
	v_add_f32_dpp v2, v2, v2 row_half_mirror row_mask:0xf bank_mask:0xf
	s_nop 1
	v_add_f32_dpp v2, v2, v2 row_mirror row_mask:0xf bank_mask:0xf
	s_nop 1
	v_add_f32_dpp v2, v2, v2 row_bcast:15 row_mask:0xa bank_mask:0xf
	s_nop 1
	v_add_f32_dpp v2, v2, v2 row_bcast:31 row_mask:0xc bank_mask:0xf
	s_nop 1
	v_readlane_b32 vcc_lo, v2, 63
	s_nop 1
	v_mov_b32_e32 v2, vcc_lo
	v_mov_b32_e32 v108, v4
	v_mov_b32_e32 v109, v6
	v_mov_b32_e32 v6, v5
	v_mov_b32_e32 v110, v8
	v_mov_b32_e32 v111, v10
	v_mov_b32_e32 v10, v9
	v_mov_b32_e32 v8, v16
	v_mov_b32_e32 v4, v12
	v_mov_b32_e32 v5, v14
	v_mov_b32_e32 v9, v18
	v_mov_b32_e32 v12, v24
	v_mov_b32_e32 v14, v13
	v_mov_b32_e32 v18, v17
	v_mov_b32_e32 v13, v26
	v_mov_b32_e32 v16, v32
	v_mov_b32_e32 v17, v34
	v_mov_b32_e32 v26, v25
	v_mov_b32_e32 v34, v33
	v_mov_b32_e32 v24, v20
	v_mov_b32_e32 v25, v22
	v_mov_b32_e32 v32, v28
	v_mov_b32_e32 v33, v30
	v_fmamk_f32 v2, v2, 0x3a800000, v237
	v_mul_f32_e32 v20, 0x4b800000, v2
	v_cmp_gt_f32_e32 vcc, s85, v2
	v_mov_b32_e32 v22, v21
	v_mov_b32_e32 v30, v29
	v_cndmask_b32_e32 v2, v2, v20, vcc
	v_rsq_f32_e32 v2, v2
	s_nop 0
	v_mul_f32_e32 v20, 0x45800000, v2
	v_cndmask_b32_e32 v2, v2, v20, vcc
	v_pk_mul_f32 v[20:21], v[70:71], v[2:3] op_sel_hi:[1,0]
	v_pk_mul_f32 v[28:29], v[74:75], v[2:3] op_sel_hi:[1,0]
	v_pk_mul_f32 v[70:71], v[72:73], v[2:3] op_sel_hi:[1,0]
	v_pk_mul_f32 v[64:65], v[64:65], v[2:3] op_sel_hi:[1,0]
	v_pk_fma_f32 v[12:13], v[12:13], v[20:21], v[16:17]
	v_pk_fma_f32 v[16:17], v[24:25], v[28:29], v[32:33]
	v_pk_fma_f32 v[20:21], v[26:27], v[70:71], v[34:35]
	v_pk_mul_f32 v[72:73], v[76:77], v[2:3] op_sel_hi:[1,0]
	v_pk_fma_f32 v[28:29], v[6:7], v[64:65], v[10:11]
	v_bfe_u32 v6, v20, 16, 1
	v_bfe_u32 v10, v17, 16, 1
	v_max3_f32 v35, |v12|, 0, |v20|
	v_pk_fma_f32 v[22:23], v[22:23], v[72:73], v[30:31]
	v_add3_u32 v53, v20, v6, s86
	v_add3_u32 v6, v17, v10, s86
	v_max3_f32 v10, v35, |v13|, |v21|
	v_pk_mul_f32 v[62:63], v[62:63], v[2:3] op_sel_hi:[1,0]
	v_max3_f32 v10, v10, |v16|, |v22|
	v_pk_fma_f32 v[24:25], v[108:109], v[62:63], v[110:111]
	v_max3_f32 v10, v10, |v17|, |v23|
	v_pk_mul_f32 v[66:67], v[66:67], v[2:3] op_sel_hi:[1,0]
	v_pk_mul_f32 v[68:69], v[68:69], v[2:3] op_sel_hi:[1,0]
	v_max3_f32 v10, v10, |v24|, |v28|
	v_pk_fma_f32 v[26:27], v[4:5], v[66:67], v[8:9]
	v_pk_fma_f32 v[14:15], v[14:15], v[68:69], v[18:19]
	v_max3_f32 v10, v10, |v25|, |v29|
	v_max3_f32 v10, v10, |v26|, |v14|
	v_max3_f32 v10, v10, |v27|, |v15|
	v_mov_b32_e32 v147, v10
	s_nop 1
	v_max_f32_dpp v147, v147, v147 quad_perm:[1,0,3,2] row_mask:0xf bank_mask:0xf
	s_nop 1
	v_max_f32_dpp v147, v147, v147 quad_perm:[2,3,0,1] row_mask:0xf bank_mask:0xf
	s_nop 1
	v_max_f32_dpp v147, v147, v147 row_half_mirror row_mask:0xf bank_mask:0xf
	s_nop 1
	v_max_f32_dpp v147, v147, v147 row_mirror row_mask:0xf bank_mask:0xf
	s_nop 1
	v_max_f32_dpp v147, v147, v147 row_bcast:15 row_mask:0xa bank_mask:0xf
	s_nop 1
	v_max_f32_dpp v147, v147, v147 row_bcast:31 row_mask:0xc bank_mask:0xf
	s_nop 1
	v_readlane_b32 vcc_lo, v147, 63
	s_nop 1
	v_mov_b32_e32 v147, vcc_lo
	v_bfe_u32 v7, v12, 16, 1
	v_add3_u32 v7, v12, v7, s86
	v_lshrrev_b32_e32 v62, 16, v7
	v_bfe_u32 v2, v23, 16, 1
	v_add3_u32 v2, v23, v2, s86
	v_lshrrev_b32_e32 v6, 16, v6
	v_bfe_u32 v8, v13, 16, 1
	v_bfe_u32 v5, v21, 16, 1
	v_add3_u32 v8, v13, v8, s86
	v_bfe_u32 v34, v27, 16, 1
	v_add3_u32 v5, v21, v5, s86
	v_lshrrev_b32_e32 v8, 16, v8
	v_and_or_b32 v7, v2, s87, v6
	v_bfe_u32 v11, v15, 16, 1
	v_add3_u32 v34, v27, v34, s86
	v_and_or_b32 v5, v5, s87, v8
	v_add3_u32 v11, v15, v11, s86
	v_lshrrev_b32_e32 v34, 16, v34
	v_and_or_b32 v11, v11, s87, v34
	v_bfe_u32 v9, v16, 16, 1
	v_bfe_u32 v4, v22, 16, 1
	v_add3_u32 v9, v16, v9, s86
	v_add3_u32 v4, v22, v4, s86
	v_lshrrev_b32_e32 v9, 16, v9
	v_and_or_b32 v6, v4, s87, v9
	v_and_or_b32 v4, v53, s87, v62
	v_max_f32_e32 v2, s55, v147
	global_store_dwordx4 v[78:79], v[4:7], off
	v_bfe_u32 v31, v24, 16, 1
	v_bfe_u32 v32, v25, 16, 1
	v_div_scale_f32 v4, s[42:43], v2, v2, s80
	v_rcp_f32_e32 v5, v4
	v_bfe_u32 v33, v26, 16, 1
	v_bfe_u32 v18, v14, 16, 1
	v_bfe_u32 v19, v29, 16, 1
	v_bfe_u32 v30, v28, 16, 1
	v_add3_u32 v33, v26, v33, s86
	v_add3_u32 v32, v25, v32, s86
	v_add3_u32 v31, v24, v31, s86
	v_fma_f32 v7, -v4, v5, 1.0
	v_add3_u32 v30, v28, v30, s86
	v_add3_u32 v19, v29, v19, s86
	v_add3_u32 v18, v14, v18, s86
	v_lshrrev_b32_e32 v31, 16, v31
	v_lshrrev_b32_e32 v32, 16, v32
	v_lshrrev_b32_e32 v33, 16, v33
	v_div_scale_f32 v6, vcc, s80, v2, s80
	v_fmac_f32_e32 v5, v7, v5
	v_and_or_b32 v10, v18, s87, v33
	v_and_or_b32 v9, v19, s87, v32
	v_and_or_b32 v8, v30, s87, v31
	v_mul_f32_e32 v7, v6, v5
	global_store_dwordx4 v[78:79], v[8:11], off offset:1024
	s_nop 1
	v_fma_f32 v8, -v4, v7, v6
	v_fmac_f32_e32 v7, v8, v5
	v_fma_f32 v4, -v4, v7, v6
	v_div_fmas_f32 v4, v4, v5, v7
	v_div_fixup_f32 v4, v4, v2, s80
	v_mul_f32_e32 v5, v12, v4
	v_mul_f32_e32 v6, v20, v4
	v_rndne_f32_e32 v5, v5
	v_mul_f32_e32 v7, v13, v4
	v_mul_f32_e32 v8, v21, v4
	v_mul_f32_e32 v9, v16, v4
	v_mul_f32_e32 v10, v22, v4
	v_mul_f32_e32 v11, v17, v4
	v_mul_f32_e32 v12, v23, v4
	v_mul_f32_e32 v13, v24, v4
	v_mul_f32_e32 v16, v28, v4
	v_mul_f32_e32 v17, v25, v4
	v_mul_f32_e32 v18, v29, v4
	v_mul_f32_e32 v19, v26, v4
	v_mul_f32_e32 v14, v14, v4
	v_mul_f32_e32 v20, v27, v4
	v_mul_f32_e32 v4, v15, v4
	v_rndne_f32_e32 v6, v6
	v_rndne_f32_e32 v15, v4
	v_add_f32_e32 v4, 0x43000000, v5
	v_rndne_f32_e32 v7, v7
	v_cvt_pk_u8_f32 v4, v4, 0, 0
	v_add_f32_e32 v5, 0x43000000, v6
	v_rndne_f32_e32 v8, v8
	v_cvt_pk_u8_f32 v4, v5, 1, v4
	v_add_f32_e32 v5, 0x43000000, v7
	v_rndne_f32_e32 v9, v9
	v_cvt_pk_u8_f32 v4, v5, 2, v4
	v_add_f32_e32 v5, 0x43000000, v8
	v_rndne_f32_e32 v10, v10
	v_cvt_pk_u8_f32 v4, v5, 3, v4
	v_add_f32_e32 v5, 0x43000000, v9
	v_rndne_f32_e32 v11, v11
	v_cvt_pk_u8_f32 v5, v5, 0, 0
	v_add_f32_e32 v6, 0x43000000, v10
	v_rndne_f32_e32 v12, v12
	v_cvt_pk_u8_f32 v5, v6, 1, v5
	v_add_f32_e32 v6, 0x43000000, v11
	v_rndne_f32_e32 v13, v13
	v_cvt_pk_u8_f32 v5, v6, 2, v5
	v_add_f32_e32 v6, 0x43000000, v12
	v_rndne_f32_e32 v16, v16
	v_cvt_pk_u8_f32 v5, v6, 3, v5
	v_add_f32_e32 v6, 0x43000000, v13
	v_rndne_f32_e32 v17, v17
	v_cvt_pk_u8_f32 v6, v6, 0, 0
	v_add_f32_e32 v7, 0x43000000, v16
	v_rndne_f32_e32 v18, v18
	v_cvt_pk_u8_f32 v6, v7, 1, v6
	v_add_f32_e32 v7, 0x43000000, v17
	v_rndne_f32_e32 v19, v19
	v_cvt_pk_u8_f32 v6, v7, 2, v6
	v_add_f32_e32 v7, 0x43000000, v18
	v_rndne_f32_e32 v14, v14
	v_cvt_pk_u8_f32 v6, v7, 3, v6
	v_add_f32_e32 v7, 0x43000000, v19
	v_rndne_f32_e32 v20, v20
	v_cvt_pk_u8_f32 v7, v7, 0, 0
	v_add_f32_e32 v8, 0x43000000, v14
	v_cvt_pk_u8_f32 v7, v8, 1, v7
	v_add_f32_e32 v8, 0x43000000, v20
	v_cvt_pk_u8_f32 v7, v8, 2, v7
	v_add_f32_e32 v8, 0x43000000, v15
	v_xor_b32_e32 v4, 0x80808080, v4
	v_xor_b32_e32 v5, 0x80808080, v5
	v_cvt_pk_u8_f32 v7, v8, 3, v7
	v_lshl_add_u64 v[8:9], s[10:11], 0, v[38:39]
	v_xor_b32_e32 v6, 0x80808080, v6
	v_xor_b32_e32 v7, 0x80808080, v7
	global_store_dwordx2 v[8:9], v[4:5], off
	global_store_dwordx2 v[8:9], v[6:7], off offset:512
	s_and_saveexec_b64 s[10:11], s[4:5]
	s_cbranch_execz .LBB0_1208
	s_add_u32 s42, s18, s14
	s_addc_u32 s43, s19, s15
	v_mul_f32_e32 v2, 0x3c010204, v2
	global_store_dword v3, v2, s[42:43]
.LBB0_1208:
	s_or_b64 exec, exec, s[10:11]
	v_lshl_add_u64 v[78:79], s[18:19], 0, v[54:55]
	v_add_co_u32_e32 v4, vcc, 0x2f200000, v78
	s_mov_b32 s41, 0x2e00000
	s_nop 0
	v_addc_co_u32_e32 v5, vcc, 0, v79, vcc
	s_waitcnt vmcnt(5)
	v_mov_b64_e32 v[8:9], v[124:125]
	v_mov_b64_e32 v[10:11], v[126:127]
	v_mov_b64_e32 v[12:13], v[128:129]
	v_mov_b64_e32 v[14:15], v[130:131]
	v_lshl_add_u64 v[124:125], s[18:19], 0, v[60:61]
	v_add_co_u32_e32 v124, vcc, 0x2f202000, v124
	s_nop 1
	v_addc_co_u32_e32 v125, vcc, 0, v125, vcc
	global_load_dwordx4 v[128:131], v[124:125], off
	global_load_dwordx4 v[124:127], v[124:125], off offset:1024
	s_nop 0
	v_mov_b64_e32 v[4:5], v[160:161]
	v_mov_b64_e32 v[6:7], v[162:163]
	v_add_co_u32_e32 v78, vcc, s41, v78
	s_add_i32 s10, s40, 3
	s_nop 0
	v_addc_co_u32_e32 v79, vcc, 0, v79, vcc
	s_add_u32 s11, s28, s8
	s_addc_u32 s41, s29, s9
	s_addk_i32 s40, 0xc003
	s_cmpk_lt_i32 s10, 0x4000
	s_mov_b32 s10, 0x3e200000
	s_cselect_b32 s10, s10, 0x45200000
	s_cselect_b32 s41, s41, 0
	s_cselect_b32 s40, s11, s40
	s_add_u32 s42, s18, s10
	s_addc_u32 s43, s19, 0
	s_lshl_b64 s[10:11], s[40:41], 10
	s_add_u32 s10, s42, s10
	s_addc_u32 s11, s43, s11
	v_lshlrev_b32_e32 v62, 16, v8
	v_lshlrev_b32_e32 v70, 16, v12
	v_and_b32_e32 v72, 0xffff0000, v12
	v_add_f32_e32 v2, 0, v70
	v_lshlrev_b32_e32 v71, 16, v13
	v_add_f32_e32 v2, v2, v72
	v_and_b32_e32 v73, 0xffff0000, v13
	v_add_f32_e32 v2, v2, v71
	v_lshlrev_b32_e32 v74, 16, v14
	v_add_f32_e32 v2, v2, v73
	v_and_b32_e32 v76, 0xffff0000, v14
	v_add_f32_e32 v2, v2, v74
	v_lshlrev_b32_e32 v75, 16, v15
	v_add_f32_e32 v2, v2, v76
	v_and_b32_e32 v77, 0xffff0000, v15
	v_add_f32_e32 v2, v2, v75
	v_add_f32_e32 v2, v2, v77
	v_and_b32_e32 v64, 0xffff0000, v8
	v_add_f32_e32 v2, v2, v62
	v_lshlrev_b32_e32 v63, 16, v9
	v_add_f32_e32 v2, v2, v64
	v_and_b32_e32 v65, 0xffff0000, v9
	v_add_f32_e32 v2, v2, v63
	v_lshlrev_b32_e32 v66, 16, v10
	v_add_f32_e32 v2, v2, v65
	v_and_b32_e32 v68, 0xffff0000, v10
	v_add_f32_e32 v2, v2, v66
	v_lshlrev_b32_e32 v67, 16, v11
	v_add_f32_e32 v2, v2, v68
	v_and_b32_e32 v69, 0xffff0000, v11
	v_add_f32_e32 v2, v2, v67
	v_add_f32_e32 v2, v2, v69
	s_nop 1
	v_add_f32_dpp v2, v2, v2 quad_perm:[1,0,3,2] row_mask:0xf bank_mask:0xf
	s_nop 1
	v_add_f32_dpp v2, v2, v2 quad_perm:[2,3,0,1] row_mask:0xf bank_mask:0xf
	s_nop 1
	v_add_f32_dpp v2, v2, v2 row_half_mirror row_mask:0xf bank_mask:0xf
	s_nop 1
	v_add_f32_dpp v2, v2, v2 row_mirror row_mask:0xf bank_mask:0xf
	s_nop 1
	v_add_f32_dpp v2, v2, v2 row_bcast:15 row_mask:0xa bank_mask:0xf
	s_nop 1
	v_add_f32_dpp v2, v2, v2 row_bcast:31 row_mask:0xc bank_mask:0xf
	s_nop 1
	v_readlane_b32 vcc_lo, v2, 63
	s_nop 1
	v_mov_b32_e32 v2, vcc_lo
	v_mov_b64_e32 v[8:9], v[164:165]
	v_mov_b64_e32 v[10:11], v[166:167]
	v_mov_b64_e32 v[12:13], v[168:169]
	v_mov_b64_e32 v[14:15], v[170:171]
	v_mov_b64_e32 v[16:17], v[172:173]
	v_mov_b64_e32 v[18:19], v[174:175]
	v_mov_b64_e32 v[20:21], v[176:177]
	v_mov_b64_e32 v[22:23], v[178:179]
	v_mov_b64_e32 v[24:25], v[180:181]
	v_mov_b64_e32 v[26:27], v[182:183]
	v_mov_b64_e32 v[28:29], v[184:185]
	v_mov_b64_e32 v[30:31], v[186:187]
	v_mov_b64_e32 v[32:33], v[188:189]
	v_mov_b64_e32 v[34:35], v[190:191]
	v_mul_f32_e32 v2, 0x3a800000, v2
	v_pk_add_f32 v[70:71], v[70:71], v[2:3] op_sel_hi:[1,0] neg_lo:[0,1] neg_hi:[0,1]
	v_pk_add_f32 v[72:73], v[72:73], v[2:3] op_sel_hi:[1,0] neg_lo:[0,1] neg_hi:[0,1]
	v_pk_mul_f32 v[108:109], v[70:71], v[70:71]
	v_pk_mul_f32 v[110:111], v[72:73], v[72:73]
	v_pk_add_f32 v[74:75], v[74:75], v[2:3] op_sel_hi:[1,0] neg_lo:[0,1] neg_hi:[0,1]
	v_pk_add_f32 v[76:77], v[76:77], v[2:3] op_sel_hi:[1,0] neg_lo:[0,1] neg_hi:[0,1]
	v_pk_add_f32 v[62:63], v[62:63], v[2:3] op_sel_hi:[1,0] neg_lo:[0,1] neg_hi:[0,1]
	v_pk_add_f32 v[64:65], v[64:65], v[2:3] op_sel_hi:[1,0] neg_lo:[0,1] neg_hi:[0,1]
	v_pk_add_f32 v[66:67], v[66:67], v[2:3] op_sel_hi:[1,0] neg_lo:[0,1] neg_hi:[0,1]
	v_pk_add_f32 v[68:69], v[68:69], v[2:3] op_sel_hi:[1,0] neg_lo:[0,1] neg_hi:[0,1]
	v_add_f32_e32 v2, v108, v110
	v_add_f32_e32 v2, v109, v2
	v_pk_mul_f32 v[112:113], v[74:75], v[74:75]
	v_add_f32_e32 v2, v111, v2
	v_pk_mul_f32 v[114:115], v[76:77], v[76:77]
	v_add_f32_e32 v2, v112, v2
	v_add_f32_e32 v2, v114, v2
	v_add_f32_e32 v2, v113, v2
	v_pk_mul_f32 v[116:117], v[62:63], v[62:63]
	v_add_f32_e32 v2, v115, v2
	v_pk_mul_f32 v[118:119], v[64:65], v[64:65]
	v_add_f32_e32 v2, v116, v2
	v_add_f32_e32 v2, v118, v2
	v_mov_b32_e32 v120, v68
	v_mov_b32_e32 v121, v66
	v_add_f32_e32 v2, v117, v2
	v_pk_mul_f32 v[120:121], v[120:121], v[120:121]
	v_add_f32_e32 v2, v119, v2
	v_mov_b32_e32 v122, v69
	v_mov_b32_e32 v123, v67
	v_add_f32_e32 v2, v121, v2
	v_pk_mul_f32 v[122:123], v[122:123], v[122:123]
	v_add_f32_e32 v2, v120, v2
	v_add_f32_e32 v2, v123, v2
	v_add_f32_e32 v2, v122, v2
	s_nop 1
	v_add_f32_dpp v2, v2, v2 quad_perm:[1,0,3,2] row_mask:0xf bank_mask:0xf
	s_nop 1
	v_add_f32_dpp v2, v2, v2 quad_perm:[2,3,0,1] row_mask:0xf bank_mask:0xf
	s_nop 1
	v_add_f32_dpp v2, v2, v2 row_half_mirror row_mask:0xf bank_mask:0xf
	s_nop 1
	v_add_f32_dpp v2, v2, v2 row_mirror row_mask:0xf bank_mask:0xf
	s_nop 1
	v_add_f32_dpp v2, v2, v2 row_bcast:15 row_mask:0xa bank_mask:0xf
	s_nop 1
	v_add_f32_dpp v2, v2, v2 row_bcast:31 row_mask:0xc bank_mask:0xf
	s_nop 1
	v_readlane_b32 vcc_lo, v2, 63
	s_nop 1
	v_mov_b32_e32 v2, vcc_lo
	v_mov_b32_e32 v108, v4
	v_mov_b32_e32 v109, v6
	v_mov_b32_e32 v6, v5
	v_mov_b32_e32 v110, v8
	v_mov_b32_e32 v111, v10
	v_mov_b32_e32 v10, v9
	v_mov_b32_e32 v8, v16
	v_mov_b32_e32 v4, v12
	v_mov_b32_e32 v5, v14
	v_mov_b32_e32 v9, v18
	v_mov_b32_e32 v12, v24
	v_mov_b32_e32 v14, v13
	v_mov_b32_e32 v18, v17
	v_mov_b32_e32 v13, v26
	v_mov_b32_e32 v16, v32
	v_mov_b32_e32 v17, v34
	v_mov_b32_e32 v26, v25
	v_mov_b32_e32 v34, v33
	v_mov_b32_e32 v24, v20
	v_mov_b32_e32 v25, v22
	v_mov_b32_e32 v32, v28
	v_mov_b32_e32 v33, v30
	v_fmamk_f32 v2, v2, 0x3a800000, v237
	v_mul_f32_e32 v20, 0x4b800000, v2
	v_cmp_gt_f32_e32 vcc, s85, v2
	v_mov_b32_e32 v22, v21
	v_mov_b32_e32 v30, v29
	v_cndmask_b32_e32 v2, v2, v20, vcc
	v_rsq_f32_e32 v2, v2
	s_nop 0
	v_mul_f32_e32 v20, 0x45800000, v2
	v_cndmask_b32_e32 v2, v2, v20, vcc
	v_pk_mul_f32 v[20:21], v[70:71], v[2:3] op_sel_hi:[1,0]
	v_pk_mul_f32 v[28:29], v[74:75], v[2:3] op_sel_hi:[1,0]
	v_pk_mul_f32 v[70:71], v[72:73], v[2:3] op_sel_hi:[1,0]
	v_pk_mul_f32 v[64:65], v[64:65], v[2:3] op_sel_hi:[1,0]
	v_pk_fma_f32 v[12:13], v[12:13], v[20:21], v[16:17]
	v_pk_fma_f32 v[16:17], v[24:25], v[28:29], v[32:33]
	v_pk_fma_f32 v[20:21], v[26:27], v[70:71], v[34:35]
	v_pk_mul_f32 v[72:73], v[76:77], v[2:3] op_sel_hi:[1,0]
	v_pk_fma_f32 v[28:29], v[6:7], v[64:65], v[10:11]
	v_bfe_u32 v6, v20, 16, 1
	v_bfe_u32 v10, v17, 16, 1
	v_max3_f32 v35, |v12|, 0, |v20|
	v_pk_fma_f32 v[22:23], v[22:23], v[72:73], v[30:31]
	v_add3_u32 v53, v20, v6, s86
	v_add3_u32 v6, v17, v10, s86
	v_max3_f32 v10, v35, |v13|, |v21|
	v_pk_mul_f32 v[62:63], v[62:63], v[2:3] op_sel_hi:[1,0]
	v_max3_f32 v10, v10, |v16|, |v22|
	v_pk_fma_f32 v[24:25], v[108:109], v[62:63], v[110:111]
	v_max3_f32 v10, v10, |v17|, |v23|
	v_pk_mul_f32 v[66:67], v[66:67], v[2:3] op_sel_hi:[1,0]
	v_pk_mul_f32 v[68:69], v[68:69], v[2:3] op_sel_hi:[1,0]
	v_max3_f32 v10, v10, |v24|, |v28|
	v_pk_fma_f32 v[26:27], v[4:5], v[66:67], v[8:9]
	v_pk_fma_f32 v[14:15], v[14:15], v[68:69], v[18:19]
	v_max3_f32 v10, v10, |v25|, |v29|
	v_max3_f32 v10, v10, |v26|, |v14|
	v_max3_f32 v10, v10, |v27|, |v15|
	v_mov_b32_e32 v147, v10
	s_nop 1
	v_max_f32_dpp v147, v147, v147 quad_perm:[1,0,3,2] row_mask:0xf bank_mask:0xf
	s_nop 1
	v_max_f32_dpp v147, v147, v147 quad_perm:[2,3,0,1] row_mask:0xf bank_mask:0xf
	s_nop 1
	v_max_f32_dpp v147, v147, v147 row_half_mirror row_mask:0xf bank_mask:0xf
	s_nop 1
	v_max_f32_dpp v147, v147, v147 row_mirror row_mask:0xf bank_mask:0xf
	s_nop 1
	v_max_f32_dpp v147, v147, v147 row_bcast:15 row_mask:0xa bank_mask:0xf
	s_nop 1
	v_max_f32_dpp v147, v147, v147 row_bcast:31 row_mask:0xc bank_mask:0xf
	s_nop 1
	v_readlane_b32 vcc_lo, v147, 63
	s_nop 1
	v_mov_b32_e32 v147, vcc_lo
	v_bfe_u32 v7, v12, 16, 1
	v_add3_u32 v7, v12, v7, s86
	v_lshrrev_b32_e32 v62, 16, v7
	v_bfe_u32 v2, v23, 16, 1
	v_add3_u32 v2, v23, v2, s86
	v_lshrrev_b32_e32 v6, 16, v6
	v_bfe_u32 v8, v13, 16, 1
	v_bfe_u32 v5, v21, 16, 1
	v_add3_u32 v8, v13, v8, s86
	v_bfe_u32 v34, v27, 16, 1
	v_add3_u32 v5, v21, v5, s86
	v_lshrrev_b32_e32 v8, 16, v8
	v_and_or_b32 v7, v2, s87, v6
	v_bfe_u32 v11, v15, 16, 1
	v_add3_u32 v34, v27, v34, s86
	v_and_or_b32 v5, v5, s87, v8
	v_add3_u32 v11, v15, v11, s86
	v_lshrrev_b32_e32 v34, 16, v34
	v_and_or_b32 v11, v11, s87, v34
	v_bfe_u32 v9, v16, 16, 1
	v_bfe_u32 v4, v22, 16, 1
	v_add3_u32 v9, v16, v9, s86
	v_add3_u32 v4, v22, v4, s86
	v_lshrrev_b32_e32 v9, 16, v9
	v_and_or_b32 v6, v4, s87, v9
	v_and_or_b32 v4, v53, s87, v62
	v_max_f32_e32 v2, s55, v147
	global_store_dwordx4 v[78:79], v[4:7], off
	v_bfe_u32 v31, v24, 16, 1
	v_bfe_u32 v32, v25, 16, 1
	v_div_scale_f32 v4, s[40:41], v2, v2, s80
	v_rcp_f32_e32 v5, v4
	v_bfe_u32 v33, v26, 16, 1
	v_bfe_u32 v18, v14, 16, 1
	v_bfe_u32 v19, v29, 16, 1
	v_bfe_u32 v30, v28, 16, 1
	v_add3_u32 v33, v26, v33, s86
	v_add3_u32 v32, v25, v32, s86
	v_add3_u32 v31, v24, v31, s86
	v_fma_f32 v7, -v4, v5, 1.0
	v_add3_u32 v30, v28, v30, s86
	v_add3_u32 v19, v29, v19, s86
	v_add3_u32 v18, v14, v18, s86
	v_lshrrev_b32_e32 v31, 16, v31
	v_lshrrev_b32_e32 v32, 16, v32
	v_lshrrev_b32_e32 v33, 16, v33
	v_div_scale_f32 v6, vcc, s80, v2, s80
	v_fmac_f32_e32 v5, v7, v5
	v_and_or_b32 v10, v18, s87, v33
	v_and_or_b32 v9, v19, s87, v32
	v_and_or_b32 v8, v30, s87, v31
	v_mul_f32_e32 v7, v6, v5
	global_store_dwordx4 v[78:79], v[8:11], off offset:1024
	s_nop 1
	v_fma_f32 v8, -v4, v7, v6
	v_fmac_f32_e32 v7, v8, v5
	v_fma_f32 v4, -v4, v7, v6
	v_div_fmas_f32 v4, v4, v5, v7
	v_div_fixup_f32 v4, v4, v2, s80
	v_mul_f32_e32 v5, v12, v4
	v_mul_f32_e32 v6, v20, v4
	v_rndne_f32_e32 v5, v5
	v_mul_f32_e32 v7, v13, v4
	v_mul_f32_e32 v8, v21, v4
	v_mul_f32_e32 v9, v16, v4
	v_mul_f32_e32 v10, v22, v4
	v_mul_f32_e32 v11, v17, v4
	v_mul_f32_e32 v12, v23, v4
	v_mul_f32_e32 v13, v24, v4
	v_mul_f32_e32 v16, v28, v4
	v_mul_f32_e32 v17, v25, v4
	v_mul_f32_e32 v18, v29, v4
	v_mul_f32_e32 v19, v26, v4
	v_mul_f32_e32 v14, v14, v4
	v_mul_f32_e32 v20, v27, v4
	v_mul_f32_e32 v4, v15, v4
	v_rndne_f32_e32 v6, v6
	v_rndne_f32_e32 v15, v4
	v_add_f32_e32 v4, 0x43000000, v5
	v_rndne_f32_e32 v7, v7
	v_cvt_pk_u8_f32 v4, v4, 0, 0
	v_add_f32_e32 v5, 0x43000000, v6
	v_rndne_f32_e32 v8, v8
	v_cvt_pk_u8_f32 v4, v5, 1, v4
	v_add_f32_e32 v5, 0x43000000, v7
	v_rndne_f32_e32 v9, v9
	v_cvt_pk_u8_f32 v4, v5, 2, v4
	v_add_f32_e32 v5, 0x43000000, v8
	v_rndne_f32_e32 v10, v10
	v_cvt_pk_u8_f32 v4, v5, 3, v4
	v_add_f32_e32 v5, 0x43000000, v9
	v_rndne_f32_e32 v11, v11
	v_cvt_pk_u8_f32 v5, v5, 0, 0
	v_add_f32_e32 v6, 0x43000000, v10
	v_rndne_f32_e32 v12, v12
	v_cvt_pk_u8_f32 v5, v6, 1, v5
	v_add_f32_e32 v6, 0x43000000, v11
	v_rndne_f32_e32 v13, v13
	v_cvt_pk_u8_f32 v5, v6, 2, v5
	v_add_f32_e32 v6, 0x43000000, v12
	v_rndne_f32_e32 v16, v16
	v_cvt_pk_u8_f32 v5, v6, 3, v5
	v_add_f32_e32 v6, 0x43000000, v13
	v_rndne_f32_e32 v17, v17
	v_cvt_pk_u8_f32 v6, v6, 0, 0
	v_add_f32_e32 v7, 0x43000000, v16
	v_rndne_f32_e32 v18, v18
	v_cvt_pk_u8_f32 v6, v7, 1, v6
	v_add_f32_e32 v7, 0x43000000, v17
	v_rndne_f32_e32 v19, v19
	v_cvt_pk_u8_f32 v6, v7, 2, v6
	v_add_f32_e32 v7, 0x43000000, v18
	v_rndne_f32_e32 v14, v14
	v_cvt_pk_u8_f32 v6, v7, 3, v6
	v_add_f32_e32 v7, 0x43000000, v19
	v_rndne_f32_e32 v20, v20
	v_cvt_pk_u8_f32 v7, v7, 0, 0
	v_add_f32_e32 v8, 0x43000000, v14
	v_cvt_pk_u8_f32 v7, v8, 1, v7
	v_add_f32_e32 v8, 0x43000000, v20
	v_cvt_pk_u8_f32 v7, v8, 2, v7
	v_add_f32_e32 v8, 0x43000000, v15
	v_xor_b32_e32 v4, 0x80808080, v4
	v_xor_b32_e32 v5, 0x80808080, v5
	v_cvt_pk_u8_f32 v7, v8, 3, v7
	v_lshl_add_u64 v[8:9], s[10:11], 0, v[38:39]
	v_xor_b32_e32 v6, 0x80808080, v6
	v_xor_b32_e32 v7, 0x80808080, v7
	global_store_dwordx2 v[8:9], v[4:5], off
	global_store_dwordx2 v[8:9], v[6:7], off offset:512
	s_and_saveexec_b64 s[10:11], s[4:5]
	s_cbranch_execz .LBB0_1201
	s_add_u32 s40, s18, s12
	s_addc_u32 s41, s19, s13
	v_mul_f32_e32 v2, 0x3c010204, v2
	global_store_dword v3, v2, s[40:41]
	s_branch .LBB0_1201

.LBB0_1524:
	s_andn2_b64 vcc, exec, s[26:27]
	s_cbranch_vccnz .Lgx_zero
	v_lshl_add_u64 v[116:117], v[6:7], 0, s[24:25]
	v_lshl_add_u64 v[118:119], v[18:19], 0, s[24:25]
	v_lshl_add_u64 v[120:121], v[22:23], 0, s[24:25]
	v_lshl_add_u64 v[122:123], v[20:21], 0, s[24:25]
	v_lshl_add_u64 v[124:125], v[16:17], 0, s[24:25]
	v_lshl_add_u64 v[126:127], v[12:13], 0, s[24:25]
	v_lshl_add_u64 v[128:129], v[8:9], 0, s[24:25]
	v_lshl_add_u64 v[130:131], v[4:5], 0, s[24:25]
	global_load_dword v132, v[116:117], off
	global_load_dword v133, v[118:119], off
	global_load_dword v134, v[120:121], off
	global_load_dword v135, v[122:123], off
	global_load_dword v136, v[124:125], off
	global_load_dword v137, v[126:127], off
	global_load_dword v138, v[128:129], off
	global_load_dword v139, v[130:131], off
	s_andn2_b64 vcc, exec, s[28:29]
	s_cbranch_vccnz .Lgx_nonorm
	global_load_dword v140, v[10:11], off
	global_load_dword v141, v[14:15], off
	global_load_dword v142, v[14:15], off offset:8
	global_load_dword v143, v[14:15], off offset:16
	global_load_dword v144, v[14:15], off offset:24
	global_load_dword v145, v[14:15], off offset:32
	global_load_dword v146, v[14:15], off offset:40
	global_load_dword v147, v[14:15], off offset:48
	s_waitcnt vmcnt(0)
	v_mul_f32_e32 v132, v132, v140
	v_mul_f32_e32 v133, v133, v141
	v_mul_f32_e32 v134, v134, v142
	v_mul_f32_e32 v135, v135, v143
	v_mul_f32_e32 v136, v136, v144
	v_mul_f32_e32 v137, v137, v145
	v_mul_f32_e32 v138, v138, v146
	v_mul_f32_e32 v139, v139, v147
.Lgx_nonorm:
	s_waitcnt vmcnt(0)
	ds_write_b32 v2, v132
	ds_write_b32 v2, v133 offset:264
	ds_write_b32 v2, v134 offset:528
	ds_write_b32 v2, v135 offset:792
	ds_write_b32 v2, v136 offset:1056
	ds_write_b32 v2, v137 offset:1320
	ds_write_b32 v2, v138 offset:1584
	ds_write_b32 v2, v139 offset:1848
	s_branch .Lgx_latch
.Lgx_zero:
	v_mov_b32_e32 v132, 0
	ds_write_b32 v2, v132
	ds_write_b32 v2, v132 offset:264
	ds_write_b32 v2, v132 offset:528
	ds_write_b32 v2, v132 offset:792
	ds_write_b32 v2, v132 offset:1056
	ds_write_b32 v2, v132 offset:1320
	ds_write_b32 v2, v132 offset:1584
	ds_write_b32 v2, v132 offset:1848
.Lgx_latch:
	s_add_u32 s24, s24, 0xc000
	s_addc_u32 s25, s25, 0
	v_add_u32_e32 v2, 0x840, v2
	v_lshl_add_u64 v[10:11], v[10:11], 0, 64
	s_cmp_lg_u32 s24, 0x30000
	v_lshl_add_u64 v[14:15], v[14:15], 0, 64
	s_cbranch_scc1 .LBB0_1524
